# GQA P*V sections: per-group lgkmcnt(0) replaced by counted waits per MFMA (full wait kept before the tile-buffer barrier), on top of v70
# speedup vs baseline: 1.0047x; 1.0047x over previous
.LBB0_846:
	ds_read_b128 v[64:67], v177 offset:49152
	ds_read_b128 v[68:71], v177 offset:57344
	ds_read_b128 v[188:191], v178 offset:49152
	ds_read_b128 v[204:207], v178 offset:57344
	ds_read_b128 v[230:233], v179 offset:49152
	ds_read_b128 v[234:237], v179 offset:57344
	v_add_f32_e32 v187, 0, v202
	v_add_f32_e32 v187, v221, v187
	s_waitcnt lgkmcnt(5)
	v_mfma_f32_32x32x16_bf16 v[80:95], v[64:67], v[126:129], 0
	v_add_f32_e32 v187, v222, v187
	v_add_f32_e32 v187, v223, v187
	v_add_f32_e32 v187, v224, v187
	v_add_f32_e32 v187, v225, v187
	v_add_f32_e32 v187, v201, v187
	v_add_f32_e32 v187, v203, v187
	v_add_f32_e32 v187, v196, v187
	s_waitcnt lgkmcnt(4)
	v_mfma_f32_32x32x16_bf16 v[64:79], v[68:71], v[126:129], 0
	v_add_f32_e32 v187, v198, v187
	v_add_f32_e32 v187, v199, v187
	v_add_f32_e32 v187, v200, v187
	v_exp_f32_e32 v142, v142
	v_add_f32_e32 v187, v193, v187
	v_exp_f32_e32 v143, v143
	v_add_f32_e32 v187, v194, v187
	s_waitcnt lgkmcnt(3)
	v_mfma_f32_32x32x16_bf16 v[80:95], v[188:191], v[122:125], v[80:95]
	v_exp_f32_e32 v140, v140
	v_add_f32_e32 v187, v195, v187
	v_exp_f32_e32 v141, v141
	v_add_f32_e32 v187, v197, v187
	v_exp_f32_e32 v134, v134
	v_add_f32_e32 v187, v142, v187
	v_exp_f32_e32 v135, v135
	s_waitcnt lgkmcnt(2)
	v_mfma_f32_32x32x16_bf16 v[64:79], v[204:207], v[122:125], v[64:79]
	ds_read_b128 v[188:191], v180 offset:49152
	ds_read_b128 v[204:207], v180 offset:57344
	v_add_f32_e32 v187, v143, v187
	v_exp_f32_e32 v132, v132
	v_add_f32_e32 v187, v140, v187
	v_exp_f32_e32 v133, v133
	v_add_f32_e32 v187, v141, v187
	v_exp_f32_e32 v130, v130
	s_waitcnt lgkmcnt(3)
	v_mfma_f32_32x32x16_bf16 v[80:95], v[230:233], v[118:121], v[80:95]
	v_add_f32_e32 v187, v134, v187
	v_exp_f32_e32 v131, v131
	v_add_f32_e32 v187, v135, v187
	v_exp_f32_e32 v144, v144
	v_add_f32_e32 v187, v132, v187
	v_exp_f32_e32 v145, v145
	v_add_f32_e32 v187, v133, v187
	s_waitcnt lgkmcnt(2)
	v_mfma_f32_32x32x16_bf16 v[64:79], v[234:237], v[118:121], v[64:79]
	ds_read_b128 v[230:233], v181 offset:49152
	ds_read_b128 v[234:237], v181 offset:57344
	v_exp_f32_e32 v138, v138
	v_add_f32_e32 v187, v130, v187
	v_exp_f32_e32 v139, v139
	v_add_f32_e32 v187, v131, v187
	v_exp_f32_e32 v136, v136
	v_add_f32_e32 v187, v144, v187
	s_waitcnt lgkmcnt(3)
	v_mfma_f32_32x32x16_bf16 v[80:95], v[188:191], v[114:117], v[80:95]
	v_exp_f32_e32 v137, v137
	v_add_f32_e32 v187, v145, v187
	v_add_f32_e32 v187, v138, v187
	v_add_f32_e32 v187, v139, v187
	v_add_f32_e32 v187, v136, v187
	v_add_f32_e32 v187, v137, v187
	v_cvt_pk_bf16_f32 v192, v193, v194
	s_waitcnt lgkmcnt(2)
	v_mfma_f32_32x32x16_bf16 v[64:79], v[204:207], v[114:117], v[64:79]
	ds_read_b128 v[188:191], v182 offset:49152
	ds_read_b128 v[204:207], v182 offset:57344
	v_cvt_pk_bf16_f32 v193, v195, v197
	v_cvt_pk_bf16_f32 v194, v142, v143
	v_cvt_pk_bf16_f32 v195, v140, v141
	v_cvt_pk_bf16_f32 v197, v132, v133
	s_nop 1
	v_permlane32_swap_b32_e32 v195, v197
	s_waitcnt lgkmcnt(3)
	v_mfma_f32_32x32x16_bf16 v[80:95], v[230:233], v[110:113], v[80:95]
	s_waitcnt lgkmcnt(2)
	v_mfma_f32_32x32x16_bf16 v[64:79], v[234:237], v[110:113], v[64:79]
	ds_read_b128 v[230:233], v183 offset:49152
	ds_read_b128 v[234:237], v183 offset:57344
	s_waitcnt lgkmcnt(3)
	v_mfma_f32_32x32x16_bf16 v[80:95], v[188:191], v[106:109], v[80:95]
	s_waitcnt lgkmcnt(2)
	v_mfma_f32_32x32x16_bf16 v[64:79], v[204:207], v[106:109], v[64:79]
	ds_read_b128 v[188:191], v184 offset:49152
	ds_read_b128 v[204:207], v184 offset:57344
	s_waitcnt lgkmcnt(3)
	v_mfma_f32_32x32x16_bf16 v[80:95], v[230:233], v[102:105], v[80:95]
	s_waitcnt lgkmcnt(2)
	v_mfma_f32_32x32x16_bf16 v[64:79], v[234:237], v[102:105], v[64:79]
	s_waitcnt lgkmcnt(1)
	v_mfma_f32_32x32x16_bf16 v[80:95], v[188:191], v[98:101], v[80:95]
	v_mov_b32_e32 v188, v187
	v_cvt_pk_bf16_f32 v190, v196, v198
	s_nop 0
	v_permlane32_swap_b32_e32 v187, v188
	v_cvt_pk_bf16_f32 v191, v199, v200
	v_permlane32_swap_b32_e32 v190, v192
	s_waitcnt lgkmcnt(0)
	v_mfma_f32_32x32x16_bf16 v[64:79], v[204:207], v[98:101], v[64:79]
	v_cvt_pk_bf16_f32 v204, v202, v221
	v_cvt_pk_bf16_f32 v205, v222, v223
	v_cvt_pk_bf16_f32 v206, v224, v225
	v_cvt_pk_bf16_f32 v207, v201, v203
	v_cvt_pk_bf16_f32 v196, v134, v135
	v_cvt_pk_bf16_f32 v198, v130, v131
	v_cvt_pk_bf16_f32 v199, v144, v145
	v_cvt_pk_bf16_f32 v200, v138, v139
	v_cvt_pk_bf16_f32 v201, v136, v137
	v_permlane32_swap_b32_e32 v204, v206
	v_permlane32_swap_b32_e32 v205, v207
	v_permlane32_swap_b32_e32 v191, v193
	v_permlane32_swap_b32_e32 v194, v196
	v_permlane32_swap_b32_e32 v198, v200
	v_permlane32_swap_b32_e32 v199, v201
	v_add_co_u32_e32 v138, vcc, s65, v166
	s_nop 1
	v_addc_co_u32_e32 v139, vcc, 0, v167, vcc
	global_load_dwordx4 v[130:133], v[166:167], off offset:512
	global_load_dwordx4 v[134:137], v[166:167], off
	global_load_dwordx4 v[142:145], v[138:139], off offset:512
	s_nop 0
	global_load_dwordx4 v[138:141], v[138:139], off
	ds_read_b64_tr_b16 v[208:209], v169 offset:0
	ds_read_b64_tr_b16 v[210:211], v169 offset:0x800
	ds_read_b64_tr_b16 v[212:213], v169 offset:0x1000
	ds_read_b64_tr_b16 v[214:215], v169 offset:0x1800
	ds_read_b64_tr_b16 v[218:219], v169 offset:0x2000
	ds_read_b64_tr_b16 v[220:221], v169 offset:0x2800
	ds_read_b64_tr_b16 v[222:223], v169 offset:0x3000
	ds_read_b64_tr_b16 v[224:225], v169 offset:0x3800
	s_nop 0
	s_waitcnt lgkmcnt(6)
	v_mfma_f32_32x32x16_bf16 v[0:15], v[204:207], v[208:211], v[0:15]
	ds_read_b64_tr_b16 v[208:209], v169 offset:0x200
	ds_read_b64_tr_b16 v[210:211], v169 offset:0xa00
	s_waitcnt lgkmcnt(6)
	v_mfma_f32_32x32x16_bf16 v[0:15], v[190:193], v[212:215], v[0:15]
	ds_read_b64_tr_b16 v[212:213], v169 offset:0x1200
	ds_read_b64_tr_b16 v[214:215], v169 offset:0x1a00
	s_waitcnt lgkmcnt(6)
	v_mfma_f32_32x32x16_bf16 v[0:15], v[194:197], v[218:221], v[0:15]
	ds_read_b64_tr_b16 v[218:219], v169 offset:0x2200
	ds_read_b64_tr_b16 v[220:221], v169 offset:0x2a00
	s_waitcnt lgkmcnt(6)
	v_mfma_f32_32x32x16_bf16 v[0:15], v[198:201], v[222:225], v[0:15]
	ds_read_b64_tr_b16 v[222:223], v169 offset:0x3200
	ds_read_b64_tr_b16 v[224:225], v169 offset:0x3a00
	s_waitcnt lgkmcnt(6)
	v_mfma_f32_32x32x16_bf16 v[48:63], v[204:207], v[208:211], v[48:63]
	ds_read_b64_tr_b16 v[208:209], v169 offset:0x400
	ds_read_b64_tr_b16 v[210:211], v169 offset:0xc00
	s_waitcnt lgkmcnt(6)
	v_mfma_f32_32x32x16_bf16 v[48:63], v[190:193], v[212:215], v[48:63]
	ds_read_b64_tr_b16 v[212:213], v169 offset:0x1400
	ds_read_b64_tr_b16 v[214:215], v169 offset:0x1c00
	s_waitcnt lgkmcnt(6)
	v_mfma_f32_32x32x16_bf16 v[48:63], v[194:197], v[218:221], v[48:63]
	ds_read_b64_tr_b16 v[218:219], v169 offset:0x2400
	ds_read_b64_tr_b16 v[220:221], v169 offset:0x2c00
	s_waitcnt lgkmcnt(6)
	v_mfma_f32_32x32x16_bf16 v[48:63], v[198:201], v[222:225], v[48:63]
	ds_read_b64_tr_b16 v[222:223], v169 offset:0x3400
	ds_read_b64_tr_b16 v[224:225], v169 offset:0x3c00
	s_waitcnt lgkmcnt(6)
	v_mfma_f32_32x32x16_bf16 v[32:47], v[204:207], v[208:211], v[32:47]
	ds_read_b64_tr_b16 v[208:209], v169 offset:0x600
	ds_read_b64_tr_b16 v[210:211], v169 offset:0xe00
	s_waitcnt lgkmcnt(6)
	v_mfma_f32_32x32x16_bf16 v[32:47], v[190:193], v[212:215], v[32:47]
	ds_read_b64_tr_b16 v[212:213], v169 offset:0x1600
	ds_read_b64_tr_b16 v[214:215], v169 offset:0x1e00
	s_waitcnt lgkmcnt(6)
	v_mfma_f32_32x32x16_bf16 v[32:47], v[194:197], v[218:221], v[32:47]
	ds_read_b64_tr_b16 v[218:219], v169 offset:0x2600
	ds_read_b64_tr_b16 v[220:221], v169 offset:0x2e00
	s_waitcnt lgkmcnt(6)
	v_mfma_f32_32x32x16_bf16 v[32:47], v[198:201], v[222:225], v[32:47]
	ds_read_b64_tr_b16 v[222:223], v169 offset:0x3600
	ds_read_b64_tr_b16 v[224:225], v169 offset:0x3e00
	s_waitcnt lgkmcnt(6)
	v_mfma_f32_32x32x16_bf16 v[16:31], v[204:207], v[208:211], v[16:31]
	v_max_f32_e32 v189, v81, v81
	s_waitcnt lgkmcnt(0)
	s_barrier
	s_waitcnt vmcnt(0)
	s_waitcnt vmcnt(3)
	ds_write_b128 v173, v[130:133]
	s_waitcnt vmcnt(1)
	ds_write_b128 v174, v[142:145]
	ds_write_b128 v175, v[134:137] offset:32768
	s_waitcnt vmcnt(0)
	ds_write_b128 v176, v[138:141] offset:32768
	v_mfma_f32_32x32x16_bf16 v[16:31], v[190:193], v[212:215], v[16:31]
	v_max_f32_e32 v190, v80, v80
	v_max_f32_e32 v189, v190, v189
	v_max3_f32 v189, v189, v82, v83
	v_max3_f32 v189, v189, v84, v85
	v_max3_f32 v189, v189, v86, v87
	v_max3_f32 v189, v189, v88, v89
	v_max3_f32 v189, v189, v90, v91
	v_max3_f32 v189, v189, v92, v93
	v_max3_f32 v189, v189, v94, v95
	v_max3_f32 v189, v189, v64, v65
	v_max3_f32 v189, v189, v66, v67
	v_max3_f32 v189, v189, v68, v69
	v_max3_f32 v189, v189, v70, v71
	v_max3_f32 v189, v189, v72, v73
	v_max3_f32 v189, v189, v74, v75
	v_max3_f32 v189, v189, v76, v77
	v_mfma_f32_32x32x16_bf16 v[16:31], v[194:197], v[218:221], v[16:31]
	v_max3_f32 v189, v189, v78, v79
	v_mov_b32_e32 v190, v189
	s_nop 1
	v_permlane32_swap_b32_e32 v189, v190
	v_max_f32_e32 v190, v190, v190
	v_max_f32_e32 v189, v189, v189
	v_max_f32_e32 v189, v189, v190
	v_sub_f32_e32 v190, v189, v186
	v_cmp_ge_f32_e32 vcc, s73, v190
	v_max_f32_e32 v190, v186, v186
	v_max_f32_e32 v189, v190, v189
	v_mfma_f32_32x32x16_bf16 v[16:31], v[198:201], v[222:225], v[16:31]
	v_sub_f32_e32 v190, v186, v189
	v_mul_f32_e32 v190, 0x3e0293ee, v190
	v_exp_f32_e32 v190, v190
	s_cmp_eq_u64 vcc, exec
	s_cselect_b64 s[4:5], -1, 0
	v_cndmask_b32_e64 v190, v190, 1.0, s[4:5]
	v_cmp_gt_f32_e32 vcc, 1.0, v190
	s_cbranch_vccz .LBB0_850
	s_and_saveexec_b64 s[8:9], s[2:3]
	ds_write_b32 v171, v190 offset:128
	s_or_b64 exec, exec, s[8:9]
	s_waitcnt lgkmcnt(0)
	v_add_u32_e32 v142, v168, v170
	ds_read_b128 v[130:133], v142 offset:224
	ds_read_b128 v[134:137], v142 offset:192
	ds_read_b128 v[138:141], v142 offset:160
	ds_read_b128 v[142:145], v142 offset:128
	s_waitcnt lgkmcnt(3)
	v_pk_mul_f32 v[12:13], v[12:13], v[130:131]
	s_waitcnt lgkmcnt(2)
	v_pk_mul_f32 v[8:9], v[8:9], v[134:135]
	s_waitcnt lgkmcnt(1)
	v_pk_mul_f32 v[4:5], v[4:5], v[138:139]
	v_pk_mul_f32 v[14:15], v[14:15], v[132:133]
	v_pk_mul_f32 v[10:11], v[10:11], v[136:137]
	v_pk_mul_f32 v[6:7], v[6:7], v[140:141]
	s_waitcnt lgkmcnt(0)
	v_pk_mul_f32 v[2:3], v[2:3], v[144:145]
	v_pk_mul_f32 v[0:1], v[0:1], v[142:143]
	v_pk_mul_f32 v[60:61], v[60:61], v[130:131]
	v_pk_mul_f32 v[56:57], v[56:57], v[134:135]
	v_pk_mul_f32 v[52:53], v[52:53], v[138:139]
	v_pk_mul_f32 v[62:63], v[62:63], v[132:133]
	v_pk_mul_f32 v[58:59], v[58:59], v[136:137]
	v_pk_mul_f32 v[54:55], v[54:55], v[140:141]
	v_pk_mul_f32 v[50:51], v[50:51], v[144:145]
	v_pk_mul_f32 v[48:49], v[48:49], v[142:143]
	v_pk_mul_f32 v[44:45], v[44:45], v[130:131]
	v_pk_mul_f32 v[40:41], v[40:41], v[134:135]
	v_pk_mul_f32 v[36:37], v[36:37], v[138:139]
	v_pk_mul_f32 v[46:47], v[46:47], v[132:133]
	v_pk_mul_f32 v[42:43], v[42:43], v[136:137]
	v_pk_mul_f32 v[38:39], v[38:39], v[140:141]
	v_pk_mul_f32 v[34:35], v[34:35], v[144:145]
	v_pk_mul_f32 v[32:33], v[32:33], v[142:143]
	v_pk_mul_f32 v[28:29], v[28:29], v[130:131]
	v_pk_mul_f32 v[24:25], v[24:25], v[134:135]
	v_pk_mul_f32 v[20:21], v[20:21], v[138:139]
	v_pk_mul_f32 v[30:31], v[30:31], v[132:133]
	v_pk_mul_f32 v[26:27], v[26:27], v[136:137]
	v_pk_mul_f32 v[22:23], v[22:23], v[140:141]
	v_pk_mul_f32 v[18:19], v[18:19], v[144:145]
	v_pk_mul_f32 v[16:17], v[16:17], v[142:143]
.LBB0_850:
	v_cndmask_b32_e64 v186, v189, v186, s[4:5]
	v_mul_f32_e32 v189, 0xbe0293ee, v186
	v_fmamk_f32 v80, v80, 0x3e0293ee, v189
	v_fmamk_f32 v81, v81, 0x3e0293ee, v189
	v_fmamk_f32 v82, v82, 0x3e0293ee, v189
	v_fmamk_f32 v83, v83, 0x3e0293ee, v189
	v_fmamk_f32 v84, v84, 0x3e0293ee, v189
	v_fmamk_f32 v85, v85, 0x3e0293ee, v189
	v_fmamk_f32 v86, v86, 0x3e0293ee, v189
	v_fmamk_f32 v87, v87, 0x3e0293ee, v189
	v_fmamk_f32 v88, v88, 0x3e0293ee, v189
	v_fmamk_f32 v89, v89, 0x3e0293ee, v189
	v_fmamk_f32 v90, v90, 0x3e0293ee, v189
	v_fmamk_f32 v91, v91, 0x3e0293ee, v189
	v_fmamk_f32 v92, v92, 0x3e0293ee, v189
	v_fmamk_f32 v93, v93, 0x3e0293ee, v189
	v_fmamk_f32 v94, v94, 0x3e0293ee, v189
	v_fmamk_f32 v95, v95, 0x3e0293ee, v189
	v_fmamk_f32 v199, v64, 0x3e0293ee, v189
	v_fmamk_f32 v200, v65, 0x3e0293ee, v189
	v_fmamk_f32 v201, v66, 0x3e0293ee, v189
	v_fmamk_f32 v202, v67, 0x3e0293ee, v189
	v_fmamk_f32 v203, v68, 0x3e0293ee, v189
	v_fmamk_f32 v192, v69, 0x3e0293ee, v189
	v_fmamk_f32 v193, v70, 0x3e0293ee, v189
	v_fmamk_f32 v194, v71, 0x3e0293ee, v189
	v_fmamk_f32 v195, v72, 0x3e0293ee, v189
	v_fmamk_f32 v196, v73, 0x3e0293ee, v189
	v_fmamk_f32 v197, v74, 0x3e0293ee, v189
	v_fmamk_f32 v198, v75, 0x3e0293ee, v189
	v_fmamk_f32 v191, v76, 0x3e0293ee, v189
	v_fmamk_f32 v221, v77, 0x3e0293ee, v189
	v_fmamk_f32 v222, v78, 0x3e0293ee, v189
	v_fmac_f32_e32 v189, 0x3e0293ee, v79
	v_exp_f32_e32 v139, v80
	v_exp_f32_e32 v141, v81
	v_exp_f32_e32 v142, v82
	v_exp_f32_e32 v143, v83
	v_exp_f32_e32 v144, v84
	v_exp_f32_e32 v145, v85
	v_exp_f32_e32 v138, v86
	v_exp_f32_e32 v140, v87
	v_exp_f32_e32 v133, v88
	v_exp_f32_e32 v135, v89
	v_exp_f32_e32 v136, v90
	v_exp_f32_e32 v137, v91
	v_exp_f32_e32 v130, v92
	v_exp_f32_e32 v131, v93
	v_exp_f32_e32 v132, v94
	v_exp_f32_e32 v134, v95
	s_waitcnt lgkmcnt(0)
	s_barrier
	ds_read_b128 v[64:67], v177 offset:32768
	ds_read_b128 v[68:71], v177 offset:40960
	ds_read_b128 v[204:207], v178 offset:32768
	ds_read_b128 v[208:211], v178 offset:40960
	ds_read_b128 v[230:233], v179 offset:32768
	ds_read_b128 v[234:237], v179 offset:40960
	v_exp_f32_e32 v215, v191
	v_add_f32_e32 v191, 0, v139
	s_waitcnt lgkmcnt(5)
	v_mfma_f32_32x32x16_bf16 v[80:95], v[64:67], v[126:129], 0
	v_add_f32_e32 v191, v141, v191
	v_add_f32_e32 v191, v142, v191
	v_add_f32_e32 v191, v143, v191
	v_add_f32_e32 v191, v144, v191
	v_add_f32_e32 v191, v145, v191
	v_add_f32_e32 v191, v138, v191
	v_add_f32_e32 v191, v140, v191
	s_waitcnt lgkmcnt(4)
	v_mfma_f32_32x32x16_bf16 v[64:79], v[68:71], v[126:129], 0
	v_add_f32_e32 v191, v133, v191
	v_add_f32_e32 v191, v135, v191
	v_add_f32_e32 v191, v136, v191
	v_add_f32_e32 v191, v137, v191
	v_add_f32_e32 v191, v130, v191
	v_add_f32_e32 v191, v131, v191
	v_add_f32_e32 v191, v132, v191
	s_waitcnt lgkmcnt(3)
	v_mfma_f32_32x32x16_bf16 v[80:95], v[204:207], v[122:125], v[80:95]
	v_add_f32_e32 v191, v134, v191
	v_exp_f32_e32 v193, v193
	v_exp_f32_e32 v212, v196
	v_exp_f32_e32 v213, v197
	v_exp_f32_e32 v214, v198
	v_exp_f32_e32 v218, v221
	v_exp_f32_e32 v219, v222
	s_waitcnt lgkmcnt(2)
	v_mfma_f32_32x32x16_bf16 v[64:79], v[208:211], v[122:125], v[64:79]
	ds_read_b128 v[204:207], v180 offset:32768
	ds_read_b128 v[208:211], v180 offset:40960
	v_exp_f32_e32 v189, v189
	v_cvt_pk_bf16_f32 v196, v144, v145
	v_cvt_pk_bf16_f32 v197, v138, v140
	v_cvt_pk_bf16_f32 v198, v133, v135
	s_waitcnt lgkmcnt(3)
	v_mfma_f32_32x32x16_bf16 v[80:95], v[230:233], v[118:121], v[80:95]
	s_waitcnt lgkmcnt(2)
	v_mfma_f32_32x32x16_bf16 v[64:79], v[234:237], v[118:121], v[64:79]
	ds_read_b128 v[230:233], v181 offset:32768
	ds_read_b128 v[234:237], v181 offset:40960
	s_waitcnt lgkmcnt(3)
	v_mfma_f32_32x32x16_bf16 v[80:95], v[204:207], v[114:117], v[80:95]
	s_waitcnt lgkmcnt(2)
	v_mfma_f32_32x32x16_bf16 v[64:79], v[208:211], v[114:117], v[64:79]
	ds_read_b128 v[204:207], v182 offset:32768
	ds_read_b128 v[208:211], v182 offset:40960
	s_waitcnt lgkmcnt(3)
	v_mfma_f32_32x32x16_bf16 v[80:95], v[230:233], v[110:113], v[80:95]
	s_waitcnt lgkmcnt(2)
	v_mfma_f32_32x32x16_bf16 v[64:79], v[234:237], v[110:113], v[64:79]
	ds_read_b128 v[230:233], v183 offset:32768
	ds_read_b128 v[234:237], v183 offset:40960
	s_waitcnt lgkmcnt(3)
	v_mfma_f32_32x32x16_bf16 v[80:95], v[204:207], v[106:109], v[80:95]
	s_waitcnt lgkmcnt(2)
	v_mfma_f32_32x32x16_bf16 v[64:79], v[208:211], v[106:109], v[64:79]
	ds_read_b128 v[204:207], v184 offset:32768
	ds_read_b128 v[208:211], v184 offset:40960
	s_waitcnt lgkmcnt(3)
	v_mfma_f32_32x32x16_bf16 v[80:95], v[230:233], v[102:105], v[80:95]
	s_waitcnt lgkmcnt(2)
	v_mfma_f32_32x32x16_bf16 v[64:79], v[234:237], v[102:105], v[64:79]
	s_waitcnt lgkmcnt(1)
	v_mfma_f32_32x32x16_bf16 v[80:95], v[204:207], v[98:101], v[80:95]
	v_exp_f32_e32 v204, v199
	v_exp_f32_e32 v205, v200
	v_exp_f32_e32 v206, v201
	v_exp_f32_e32 v207, v202
	v_add_f32_e32 v191, v204, v191
	v_add_f32_e32 v191, v205, v191
	v_add_f32_e32 v191, v206, v191
	s_waitcnt lgkmcnt(0)
	v_mfma_f32_32x32x16_bf16 v[64:79], v[208:211], v[98:101], v[64:79]
	v_exp_f32_e32 v208, v203
	v_exp_f32_e32 v209, v192
	v_exp_f32_e32 v210, v194
	v_add_f32_e32 v191, v207, v191
	v_exp_f32_e32 v211, v195
	v_add_f32_e32 v191, v208, v191
	v_add_f32_e32 v191, v209, v191
	v_add_f32_e32 v191, v193, v191
	v_add_f32_e32 v191, v210, v191
	v_add_f32_e32 v191, v211, v191
	v_add_f32_e32 v191, v212, v191
	v_add_f32_e32 v191, v213, v191
	v_add_f32_e32 v191, v214, v191
	v_add_f32_e32 v191, v215, v191
	v_add_f32_e32 v191, v218, v191
	v_add_f32_e32 v191, v219, v191
	v_add_f32_e32 v191, v189, v191
	v_mov_b32_e32 v192, v191
	s_nop 1
	v_permlane32_swap_b32_e32 v191, v192
	v_cvt_pk_bf16_f32 v194, v139, v141
	v_cvt_pk_bf16_f32 v195, v142, v143
	v_cvt_pk_bf16_f32 v199, v136, v137
	v_cvt_pk_bf16_f32 v200, v130, v131
	v_cvt_pk_bf16_f32 v201, v132, v134
	v_cvt_pk_bf16_f32 v202, v204, v205
	v_cvt_pk_bf16_f32 v203, v206, v207
	v_cvt_pk_bf16_f32 v204, v208, v209
	v_cvt_pk_bf16_f32 v205, v193, v210
	v_cvt_pk_bf16_f32 v206, v211, v212
	v_cvt_pk_bf16_f32 v207, v213, v214
	v_cvt_pk_bf16_f32 v208, v215, v218
	v_cvt_pk_bf16_f32 v209, v219, v189
	v_permlane32_swap_b32_e32 v194, v196
	v_permlane32_swap_b32_e32 v195, v197
	v_permlane32_swap_b32_e32 v198, v200
	v_permlane32_swap_b32_e32 v199, v201
	v_permlane32_swap_b32_e32 v202, v204
	v_permlane32_swap_b32_e32 v203, v205
	v_permlane32_swap_b32_e32 v206, v208
	v_permlane32_swap_b32_e32 v207, v209
	v_add_co_u32_e32 v134, vcc, s49, v166
	s_nop 1
	v_addc_co_u32_e32 v135, vcc, 0, v167, vcc
	v_add_co_u32_e32 v138, vcc, s64, v166
	s_nop 1
	v_addc_co_u32_e32 v139, vcc, 0, v167, vcc
	global_load_dwordx4 v[130:133], v[134:135], off offset:512
	s_nop 0
	global_load_dwordx4 v[134:137], v[134:135], off
	s_nop 0
	global_load_dwordx4 v[142:145], v[138:139], off offset:512
	s_nop 0
	global_load_dwordx4 v[138:141], v[138:139], off
	ds_read_b64_tr_b16 v[210:211], v172 offset:0
	ds_read_b64_tr_b16 v[212:213], v172 offset:0x800
	ds_read_b64_tr_b16 v[218:219], v172 offset:0x1000
	ds_read_b64_tr_b16 v[220:221], v172 offset:0x1800
	ds_read_b64_tr_b16 v[222:223], v172 offset:0x2000
	ds_read_b64_tr_b16 v[224:225], v172 offset:0x2800
	ds_read_b64_tr_b16 v[226:227], v172 offset:0x3000
	ds_read_b64_tr_b16 v[228:229], v172 offset:0x3800
	s_nop 0
	s_waitcnt lgkmcnt(6)
	v_mfma_f32_32x32x16_bf16 v[0:15], v[194:197], v[210:213], v[0:15]
	ds_read_b64_tr_b16 v[210:211], v172 offset:0x200
	ds_read_b64_tr_b16 v[212:213], v172 offset:0xa00
	s_waitcnt lgkmcnt(6)
	v_mfma_f32_32x32x16_bf16 v[0:15], v[198:201], v[218:221], v[0:15]
	ds_read_b64_tr_b16 v[218:219], v172 offset:0x1200
	ds_read_b64_tr_b16 v[220:221], v172 offset:0x1a00
	s_waitcnt lgkmcnt(6)
	v_mfma_f32_32x32x16_bf16 v[0:15], v[202:205], v[222:225], v[0:15]
	ds_read_b64_tr_b16 v[222:223], v172 offset:0x2200
	ds_read_b64_tr_b16 v[224:225], v172 offset:0x2a00
	s_waitcnt lgkmcnt(6)
	v_mfma_f32_32x32x16_bf16 v[0:15], v[206:209], v[226:229], v[0:15]
	ds_read_b64_tr_b16 v[226:227], v172 offset:0x3200
	ds_read_b64_tr_b16 v[228:229], v172 offset:0x3a00
	s_waitcnt lgkmcnt(6)
	v_mfma_f32_32x32x16_bf16 v[48:63], v[194:197], v[210:213], v[48:63]
	ds_read_b64_tr_b16 v[210:211], v172 offset:0x400
	ds_read_b64_tr_b16 v[212:213], v172 offset:0xc00
	s_waitcnt lgkmcnt(6)
	v_mfma_f32_32x32x16_bf16 v[48:63], v[198:201], v[218:221], v[48:63]
	ds_read_b64_tr_b16 v[218:219], v172 offset:0x1400
	ds_read_b64_tr_b16 v[220:221], v172 offset:0x1c00
	s_waitcnt lgkmcnt(6)
	v_mfma_f32_32x32x16_bf16 v[48:63], v[202:205], v[222:225], v[48:63]
	ds_read_b64_tr_b16 v[222:223], v172 offset:0x2400
	ds_read_b64_tr_b16 v[224:225], v172 offset:0x2c00
	s_waitcnt lgkmcnt(6)
	v_mfma_f32_32x32x16_bf16 v[48:63], v[206:209], v[226:229], v[48:63]
	ds_read_b64_tr_b16 v[226:227], v172 offset:0x3400
	ds_read_b64_tr_b16 v[228:229], v172 offset:0x3c00
	s_waitcnt lgkmcnt(6)
	v_mfma_f32_32x32x16_bf16 v[32:47], v[194:197], v[210:213], v[32:47]
	ds_read_b64_tr_b16 v[210:211], v172 offset:0x600
	ds_read_b64_tr_b16 v[212:213], v172 offset:0xe00
	s_waitcnt lgkmcnt(6)
	v_mfma_f32_32x32x16_bf16 v[32:47], v[198:201], v[218:221], v[32:47]
	ds_read_b64_tr_b16 v[218:219], v172 offset:0x1600
	ds_read_b64_tr_b16 v[220:221], v172 offset:0x1e00
	s_waitcnt lgkmcnt(6)
	v_mfma_f32_32x32x16_bf16 v[32:47], v[202:205], v[222:225], v[32:47]
	ds_read_b64_tr_b16 v[222:223], v172 offset:0x2600
	ds_read_b64_tr_b16 v[224:225], v172 offset:0x2e00
	s_waitcnt lgkmcnt(6)
	v_mfma_f32_32x32x16_bf16 v[32:47], v[206:209], v[226:229], v[32:47]
	ds_read_b64_tr_b16 v[226:227], v172 offset:0x3600
	ds_read_b64_tr_b16 v[228:229], v172 offset:0x3e00
	s_waitcnt lgkmcnt(6)
	v_mfma_f32_32x32x16_bf16 v[16:31], v[194:197], v[210:213], v[16:31]
	v_max_f32_e32 v189, v81, v81
	v_max_f32_e32 v193, v80, v80
	v_max_f32_e32 v189, v193, v189
	v_max3_f32 v189, v189, v82, v83
	v_max3_f32 v189, v189, v84, v85
	v_max3_f32 v189, v189, v86, v87
	v_max3_f32 v189, v189, v88, v89
	v_max3_f32 v189, v189, v90, v91
	v_max3_f32 v189, v189, v92, v93
	s_waitcnt lgkmcnt(4)
	v_mfma_f32_32x32x16_bf16 v[16:31], v[198:201], v[218:221], v[16:31]
	v_max3_f32 v189, v189, v94, v95
	v_max3_f32 v189, v189, v64, v65
	v_max3_f32 v189, v189, v66, v67
	v_max3_f32 v189, v189, v68, v69
	v_max3_f32 v189, v189, v70, v71
	v_max3_f32 v189, v189, v72, v73
	v_max3_f32 v189, v189, v74, v75
	v_max3_f32 v189, v189, v76, v77
	s_waitcnt lgkmcnt(2)
	v_mfma_f32_32x32x16_bf16 v[16:31], v[202:205], v[222:225], v[16:31]
	v_max3_f32 v189, v189, v78, v79
	v_mov_b32_e32 v193, v189
	s_nop 1
	v_permlane32_swap_b32_e32 v189, v193
	v_max_f32_e32 v193, v193, v193
	v_max_f32_e32 v189, v189, v189
	v_max_f32_e32 v189, v189, v193
	v_sub_f32_e32 v193, v189, v186
	v_cmp_ge_f32_e32 vcc, s73, v193
	v_max_f32_e32 v193, v186, v186
	v_max_f32_e32 v193, v193, v189
	s_waitcnt lgkmcnt(0)
	v_mfma_f32_32x32x16_bf16 v[16:31], v[206:209], v[226:229], v[16:31]
	v_sub_f32_e32 v189, v186, v193
	v_mul_f32_e32 v189, 0x3e0293ee, v189
	v_exp_f32_e32 v189, v189
	s_cmp_eq_u64 vcc, exec
	s_cselect_b64 s[4:5], -1, 0
	s_barrier
	s_waitcnt vmcnt(0)
	v_cndmask_b32_e64 v189, v189, 1.0, s[4:5]
	v_cmp_gt_f32_e32 vcc, 1.0, v189
	s_waitcnt vmcnt(3)
	ds_write_b128 v173, v[130:133] offset:16384
	s_waitcnt vmcnt(1)
	ds_write_b128 v174, v[142:145] offset:16384
	ds_write_b128 v175, v[134:137] offset:49152
	s_waitcnt vmcnt(0)
	ds_write_b128 v176, v[138:141] offset:49152
	s_cbranch_vccz .LBB0_854
	s_and_saveexec_b64 s[8:9], s[2:3]
	ds_write_b32 v171, v189 offset:128
	s_or_b64 exec, exec, s[8:9]
	s_waitcnt lgkmcnt(0)
	v_add_u32_e32 v142, v168, v170
	ds_read_b128 v[130:133], v142 offset:224
	ds_read_b128 v[134:137], v142 offset:192
	ds_read_b128 v[138:141], v142 offset:160
	ds_read_b128 v[142:145], v142 offset:128
	s_waitcnt lgkmcnt(3)
	v_pk_mul_f32 v[12:13], v[12:13], v[130:131]
	s_waitcnt lgkmcnt(2)
	v_pk_mul_f32 v[8:9], v[8:9], v[134:135]
	s_waitcnt lgkmcnt(1)
	v_pk_mul_f32 v[4:5], v[4:5], v[138:139]
	v_pk_mul_f32 v[14:15], v[14:15], v[132:133]
	v_pk_mul_f32 v[10:11], v[10:11], v[136:137]
	v_pk_mul_f32 v[6:7], v[6:7], v[140:141]
	s_waitcnt lgkmcnt(0)
	v_pk_mul_f32 v[2:3], v[2:3], v[144:145]
	v_pk_mul_f32 v[0:1], v[0:1], v[142:143]
	v_pk_mul_f32 v[60:61], v[60:61], v[130:131]
	v_pk_mul_f32 v[56:57], v[56:57], v[134:135]
	v_pk_mul_f32 v[52:53], v[52:53], v[138:139]
	v_pk_mul_f32 v[62:63], v[62:63], v[132:133]
	v_pk_mul_f32 v[58:59], v[58:59], v[136:137]
	v_pk_mul_f32 v[54:55], v[54:55], v[140:141]
	v_pk_mul_f32 v[50:51], v[50:51], v[144:145]
	v_pk_mul_f32 v[48:49], v[48:49], v[142:143]
	v_pk_mul_f32 v[44:45], v[44:45], v[130:131]
	v_pk_mul_f32 v[40:41], v[40:41], v[134:135]
	v_pk_mul_f32 v[36:37], v[36:37], v[138:139]
	v_pk_mul_f32 v[46:47], v[46:47], v[132:133]
	v_pk_mul_f32 v[42:43], v[42:43], v[136:137]
	v_pk_mul_f32 v[38:39], v[38:39], v[140:141]
	v_pk_mul_f32 v[34:35], v[34:35], v[144:145]
	v_pk_mul_f32 v[32:33], v[32:33], v[142:143]
	v_pk_mul_f32 v[28:29], v[28:29], v[130:131]
	v_pk_mul_f32 v[24:25], v[24:25], v[134:135]
	v_pk_mul_f32 v[20:21], v[20:21], v[138:139]
	v_pk_mul_f32 v[30:31], v[30:31], v[132:133]
	v_pk_mul_f32 v[26:27], v[26:27], v[136:137]
	v_pk_mul_f32 v[22:23], v[22:23], v[140:141]
	v_pk_mul_f32 v[18:19], v[18:19], v[144:145]
	v_pk_mul_f32 v[16:17], v[16:17], v[142:143]
